# gate_up: hand-written SwiGLU epilogue + epilogues no longer barrier-aligned (leading half's epilogue overlaps the trailing half's last MFMA block; stagger carried across units, undone at the phase dra
# speedup vs baseline: 1.0032x; 1.0032x over previous
; #define PG8_LAS __attribute__((address_space(3)))
; __device__ __forceinline__ float sigm(float x) { return __builtin_amdgcn_rcpf(1.0f + __builtin_amdgcn_exp2f(-1.4426950408889634f * x)); }
; __device__ __forceinline__ u32x4 pack8(const f32x4 a, const f32x4 b) { u32x4 w; w.x = cvt_pk_bf16(a[0], a[1]); w.y = cvt_pk_bf16(a[2], a[3]); w.z = cvt_pk_bf16(b[0], b[1]); w.w = cvt_pk_bf16(b[2], b[3]); return w; }
; #define PG8_BAR __builtin_amdgcn_s_barrier()
;     __device__ __forceinline__ void operator()(const f32x4 (&acc)[2][2][4][2], const Unit& u, int wr, int wc, int fr, int fq) const {
;         const int rl0 = wr * 64 + fr + (u.half == 2 ? HALF : 0), row0 = u.pm * BM + rl0, col0 = u.pn * HALF + wc * 32 + 8 * fq; const PG8_LAS float* rsr = rsl + rl0;
; #pragma unroll
;         for (int ai = 0; ai < 2; ++ai) { if (ai == 1 && u.half != 0) break;
; #pragma unroll
;             for (int m = 0; m < 4; ++m) { const float rf = rsr[ai * HALF + m * 16]; f32x4 v0 = acc[ai][0][m][0] * rf, v1 = acc[ai][0][m][1] * rf; const f32x4 u0 = acc[ai][1][m][0] * rf, u1 = acc[ai][1][m][1] * rf;
; #pragma unroll
;                 for (int e = 0; e < 4; ++e) { v0[e] = v0[e] * sigm(v0[e]) * u0[e]; v1[e] = v1[e] * sigm(v1[e]) * u1[e]; }
;                 *(u32x4*)(H + (size_t)(row0 + ai * HALF + m * 16) * DFF + col0) = pack8(v0, v1); } }
;     }
; template <class Epi, class Sched, bool ALIGN_EPI = false, bool SP2 = false>
; __device__ __forceinline__ void gemm_phase(PG8_LAS unsigned char* lds, const Gemm g, const Sched& S, const Epi& E) {
;     ...
;         if constexpr (ALIGN_EPI) { if (wr == 0) PG8_BAR; }
.LBB0_1480:
	ds_read_b32 v236, v148
	v_lshl_or_b32 v244, s20, 7, v149
	v_lshl_add_u32 v228, s14, 8, v146
	v_ashrrev_i32_e32 v245, 31, v244
	v_mov_b64_e32 v[240:241], s[4:5]
	v_mad_i64_i32 v[240:241], s[0:1], v228, s2, v[240:241]
	v_lshlrev_b64 v[244:245], 1, v[244:245]
	v_lshl_add_u64 v[240:241], v[240:241], 0, v[244:245]
	s_waitcnt lgkmcnt(0)
	ds_read_b32 v239, v148 offset:64
	v_mul_f32_e32 v237, 0xbfb8aa3b, v236
	v_mul_f32_e32 v238, v236, v236
	v_rcp_f32_e32 v238, v238
	v_mul_f32_e32 v228, v237, v128
	v_mul_f32_e32 v229, v237, v129
	v_mul_f32_e32 v230, v237, v130
	v_mul_f32_e32 v231, v237, v131
	v_mul_f32_e32 v232, v237, v124
	v_mul_f32_e32 v233, v237, v125
	v_mul_f32_e32 v234, v237, v126
	v_mul_f32_e32 v235, v237, v127
	v_exp_f32_e32 v228, v228
	v_exp_f32_e32 v229, v229
	v_exp_f32_e32 v230, v230
	v_exp_f32_e32 v231, v231
	v_exp_f32_e32 v232, v232
	v_exp_f32_e32 v233, v233
	v_exp_f32_e32 v234, v234
	v_exp_f32_e32 v235, v235
	v_fma_f32 v228, v228, v238, v238
	v_fma_f32 v229, v229, v238, v238
	v_fma_f32 v230, v230, v238, v238
	v_fma_f32 v231, v231, v238, v238
	v_fma_f32 v232, v232, v238, v238
	v_fma_f32 v233, v233, v238, v238
	v_fma_f32 v234, v234, v238, v238
	v_fma_f32 v235, v235, v238, v238
	v_rcp_f32_e32 v228, v228
	v_rcp_f32_e32 v229, v229
	v_rcp_f32_e32 v230, v230
	v_rcp_f32_e32 v231, v231
	v_rcp_f32_e32 v232, v232
	v_rcp_f32_e32 v233, v233
	v_rcp_f32_e32 v234, v234
	v_rcp_f32_e32 v235, v235
	v_mul_f32_e32 v120, v128, v120
	v_mul_f32_e32 v121, v129, v121
	v_mul_f32_e32 v122, v130, v122
	v_mul_f32_e32 v123, v131, v123
	v_mul_f32_e32 v116, v124, v116
	v_mul_f32_e32 v117, v125, v117
	v_mul_f32_e32 v118, v126, v118
	v_mul_f32_e32 v119, v127, v119
	v_mul_f32_e32 v128, v120, v228
	v_mul_f32_e32 v129, v121, v229
	v_mul_f32_e32 v130, v122, v230
	v_mul_f32_e32 v131, v123, v231
	v_mul_f32_e32 v124, v116, v232
	v_mul_f32_e32 v125, v117, v233
	v_mul_f32_e32 v126, v118, v234
	v_mul_f32_e32 v127, v119, v235
	v_cvt_pk_bf16_f32 v128, v128, v129
	v_cvt_pk_bf16_f32 v129, v130, v131
	v_cvt_pk_bf16_f32 v130, v124, v125
	v_cvt_pk_bf16_f32 v131, v126, v127
	global_store_dwordx4 v[240:241], v[128:131], off
	s_waitcnt lgkmcnt(0)
	v_mov_b32_e32 v236, v239
	ds_read_b32 v239, v148 offset:128
	v_mul_f32_e32 v237, 0xbfb8aa3b, v236
	v_mul_f32_e32 v238, v236, v236
	v_rcp_f32_e32 v238, v238
	v_mul_f32_e32 v228, v237, v112
	v_mul_f32_e32 v229, v237, v113
	v_mul_f32_e32 v230, v237, v114
	v_mul_f32_e32 v231, v237, v115
	v_mul_f32_e32 v232, v237, v108
	v_mul_f32_e32 v233, v237, v109
	v_mul_f32_e32 v234, v237, v110
	v_mul_f32_e32 v235, v237, v111
	v_exp_f32_e32 v228, v228
	v_exp_f32_e32 v229, v229
	v_exp_f32_e32 v230, v230
	v_exp_f32_e32 v231, v231
	v_exp_f32_e32 v232, v232
	v_exp_f32_e32 v233, v233
	v_exp_f32_e32 v234, v234
	v_exp_f32_e32 v235, v235
	v_fma_f32 v228, v228, v238, v238
	v_fma_f32 v229, v229, v238, v238
	v_fma_f32 v230, v230, v238, v238
	v_fma_f32 v231, v231, v238, v238
	v_fma_f32 v232, v232, v238, v238
	v_fma_f32 v233, v233, v238, v238
	v_fma_f32 v234, v234, v238, v238
	v_fma_f32 v235, v235, v238, v238
	v_rcp_f32_e32 v228, v228
	v_rcp_f32_e32 v229, v229
	v_rcp_f32_e32 v230, v230
	v_rcp_f32_e32 v231, v231
	v_rcp_f32_e32 v232, v232
	v_rcp_f32_e32 v233, v233
	v_rcp_f32_e32 v234, v234
	v_rcp_f32_e32 v235, v235
	v_mul_f32_e32 v104, v112, v104
	v_mul_f32_e32 v105, v113, v105
	v_mul_f32_e32 v106, v114, v106
	v_mul_f32_e32 v107, v115, v107
	v_mul_f32_e32 v100, v108, v100
	v_mul_f32_e32 v101, v109, v101
	v_mul_f32_e32 v102, v110, v102
	v_mul_f32_e32 v103, v111, v103
	s_mov_b64 s[0:1], 0x16000
	v_lshl_add_u64 v[242:243], v[240:241], 0, s[0:1]
	v_mul_f32_e32 v112, v104, v228
	v_mul_f32_e32 v113, v105, v229
	v_mul_f32_e32 v114, v106, v230
	v_mul_f32_e32 v115, v107, v231
	v_mul_f32_e32 v108, v100, v232
	v_mul_f32_e32 v109, v101, v233
	v_mul_f32_e32 v110, v102, v234
	v_mul_f32_e32 v111, v103, v235
	v_cvt_pk_bf16_f32 v112, v112, v113
	v_cvt_pk_bf16_f32 v113, v114, v115
	v_cvt_pk_bf16_f32 v114, v108, v109
	v_cvt_pk_bf16_f32 v115, v110, v111
	global_store_dwordx4 v[242:243], v[112:115], off
	s_waitcnt lgkmcnt(0)
	v_mov_b32_e32 v236, v239
	ds_read_b32 v239, v148 offset:192
	v_mul_f32_e32 v237, 0xbfb8aa3b, v236
	v_mul_f32_e32 v238, v236, v236
	v_rcp_f32_e32 v238, v238
	v_mul_f32_e32 v228, v237, v96
	v_mul_f32_e32 v229, v237, v97
	v_mul_f32_e32 v230, v237, v98
	v_mul_f32_e32 v231, v237, v99
	v_mul_f32_e32 v232, v237, v92
	v_mul_f32_e32 v233, v237, v93
	v_mul_f32_e32 v234, v237, v94
	v_mul_f32_e32 v235, v237, v95
	v_exp_f32_e32 v228, v228
	v_exp_f32_e32 v229, v229
	v_exp_f32_e32 v230, v230
	v_exp_f32_e32 v231, v231
	v_exp_f32_e32 v232, v232
	v_exp_f32_e32 v233, v233
	v_exp_f32_e32 v234, v234
	v_exp_f32_e32 v235, v235
	v_fma_f32 v228, v228, v238, v238
	v_fma_f32 v229, v229, v238, v238
	v_fma_f32 v230, v230, v238, v238
	v_fma_f32 v231, v231, v238, v238
	v_fma_f32 v232, v232, v238, v238
	v_fma_f32 v233, v233, v238, v238
	v_fma_f32 v234, v234, v238, v238
	v_fma_f32 v235, v235, v238, v238
	v_rcp_f32_e32 v228, v228
	v_rcp_f32_e32 v229, v229
	v_rcp_f32_e32 v230, v230
	v_rcp_f32_e32 v231, v231
	v_rcp_f32_e32 v232, v232
	v_rcp_f32_e32 v233, v233
	v_rcp_f32_e32 v234, v234
	v_rcp_f32_e32 v235, v235
	v_mul_f32_e32 v88, v96, v88
	v_mul_f32_e32 v89, v97, v89
	v_mul_f32_e32 v90, v98, v90
	v_mul_f32_e32 v91, v99, v91
	v_mul_f32_e32 v84, v92, v84
	v_mul_f32_e32 v85, v93, v85
	v_mul_f32_e32 v86, v94, v86
	v_mul_f32_e32 v87, v95, v87
	s_mov_b64 s[0:1], 0x2c000
	v_lshl_add_u64 v[242:243], v[240:241], 0, s[0:1]
	v_mul_f32_e32 v96, v88, v228
	v_mul_f32_e32 v97, v89, v229
	v_mul_f32_e32 v98, v90, v230
	v_mul_f32_e32 v99, v91, v231
	v_mul_f32_e32 v92, v84, v232
	v_mul_f32_e32 v93, v85, v233
	v_mul_f32_e32 v94, v86, v234
	v_mul_f32_e32 v95, v87, v235
	v_cvt_pk_bf16_f32 v96, v96, v97
	v_cvt_pk_bf16_f32 v97, v98, v99
	v_cvt_pk_bf16_f32 v98, v92, v93
	v_cvt_pk_bf16_f32 v99, v94, v95
	global_store_dwordx4 v[242:243], v[96:99], off
	s_waitcnt lgkmcnt(0)
; #define PG8_LAS __attribute__((address_space(3)))
; __device__ __forceinline__ float sigm(float x) { return __builtin_amdgcn_rcpf(1.0f + __builtin_amdgcn_exp2f(-1.4426950408889634f * x)); }
; __device__ __forceinline__ u32x4 pack8(const f32x4 a, const f32x4 b) { u32x4 w; w.x = cvt_pk_bf16(a[0], a[1]); w.y = cvt_pk_bf16(a[2], a[3]); w.z = cvt_pk_bf16(b[0], b[1]); w.w = cvt_pk_bf16(b[2], b[3]); return w; }
;     __device__ __forceinline__ void operator()(const f32x4 (&acc)[2][2][4][2], const Unit& u, int wr, int wc, int fr, int fq) const {
;         const int rl0 = wr * 64 + fr + (u.half == 2 ? HALF : 0), row0 = u.pm * BM + rl0, col0 = u.pn * HALF + wc * 32 + 8 * fq; const PG8_LAS float* rsr = rsl + rl0;
; #pragma unroll
;         for (int ai = 0; ai < 2; ++ai) { if (ai == 1 && u.half != 0) break;
; #pragma unroll
;             for (int m = 0; m < 4; ++m) { const float rf = rsr[ai * HALF + m * 16]; f32x4 v0 = acc[ai][0][m][0] * rf, v1 = acc[ai][0][m][1] * rf; const f32x4 u0 = acc[ai][1][m][0] * rf, u1 = acc[ai][1][m][1] * rf;
; #pragma unroll
;                 for (int e = 0; e < 4; ++e) { v0[e] = v0[e] * sigm(v0[e]) * u0[e]; v1[e] = v1[e] * sigm(v1[e]) * u1[e]; }
;                 *(u32x4*)(H + (size_t)(row0 + ai * HALF + m * 16) * DFF + col0) = pack8(v0, v1); } }
;     }
	v_mov_b32_e32 v236, v239
	ds_read_b32 v239, v148 offset:512
	v_mul_f32_e32 v237, 0xbfb8aa3b, v236
	v_mul_f32_e32 v238, v236, v236
	v_rcp_f32_e32 v238, v238
	v_mul_f32_e32 v228, v237, v80
	v_mul_f32_e32 v229, v237, v81
	v_mul_f32_e32 v230, v237, v82
	v_mul_f32_e32 v231, v237, v83
	v_mul_f32_e32 v232, v237, v76
	v_mul_f32_e32 v233, v237, v77
	v_mul_f32_e32 v234, v237, v78
	v_mul_f32_e32 v235, v237, v79
	v_exp_f32_e32 v228, v228
	v_exp_f32_e32 v229, v229
	v_exp_f32_e32 v230, v230
	v_exp_f32_e32 v231, v231
	v_exp_f32_e32 v232, v232
	v_exp_f32_e32 v233, v233
	v_exp_f32_e32 v234, v234
	v_exp_f32_e32 v235, v235
	v_fma_f32 v228, v228, v238, v238
	v_fma_f32 v229, v229, v238, v238
	v_fma_f32 v230, v230, v238, v238
	v_fma_f32 v231, v231, v238, v238
	v_fma_f32 v232, v232, v238, v238
	v_fma_f32 v233, v233, v238, v238
	v_fma_f32 v234, v234, v238, v238
	v_fma_f32 v235, v235, v238, v238
	v_rcp_f32_e32 v228, v228
	v_rcp_f32_e32 v229, v229
	v_rcp_f32_e32 v230, v230
	v_rcp_f32_e32 v231, v231
	v_rcp_f32_e32 v232, v232
	v_rcp_f32_e32 v233, v233
	v_rcp_f32_e32 v234, v234
	v_rcp_f32_e32 v235, v235
	v_mul_f32_e32 v72, v80, v72
	v_mul_f32_e32 v73, v81, v73
	v_mul_f32_e32 v74, v82, v74
	v_mul_f32_e32 v75, v83, v75
	v_mul_f32_e32 v68, v76, v68
	v_mul_f32_e32 v69, v77, v69
	v_mul_f32_e32 v70, v78, v70
	v_mul_f32_e32 v71, v79, v71
	s_mov_b64 s[0:1], 0x42000
	v_lshl_add_u64 v[242:243], v[240:241], 0, s[0:1]
	v_mul_f32_e32 v80, v72, v228
	v_mul_f32_e32 v81, v73, v229
	v_mul_f32_e32 v82, v74, v230
	v_mul_f32_e32 v83, v75, v231
	v_mul_f32_e32 v76, v68, v232
	v_mul_f32_e32 v77, v69, v233
	v_mul_f32_e32 v78, v70, v234
	v_mul_f32_e32 v79, v71, v235
	v_cvt_pk_bf16_f32 v80, v80, v81
	v_cvt_pk_bf16_f32 v81, v82, v83
	v_cvt_pk_bf16_f32 v82, v76, v77
	v_cvt_pk_bf16_f32 v83, v78, v79
	global_store_dwordx4 v[242:243], v[80:83], off
	s_waitcnt lgkmcnt(0)
	v_mov_b32_e32 v236, v239
	ds_read_b32 v239, v148 offset:576
	v_mul_f32_e32 v237, 0xbfb8aa3b, v236
	v_mul_f32_e32 v238, v236, v236
	v_rcp_f32_e32 v238, v238
	v_mul_f32_e32 v228, v237, v64
	v_mul_f32_e32 v229, v237, v65
	v_mul_f32_e32 v230, v237, v66
	v_mul_f32_e32 v231, v237, v67
	v_mul_f32_e32 v232, v237, v60
	v_mul_f32_e32 v233, v237, v61
	v_mul_f32_e32 v234, v237, v62
	v_mul_f32_e32 v235, v237, v63
	v_exp_f32_e32 v228, v228
	v_exp_f32_e32 v229, v229
	v_exp_f32_e32 v230, v230
	v_exp_f32_e32 v231, v231
	v_exp_f32_e32 v232, v232
	v_exp_f32_e32 v233, v233
	v_exp_f32_e32 v234, v234
	v_exp_f32_e32 v235, v235
	v_fma_f32 v228, v228, v238, v238
	v_fma_f32 v229, v229, v238, v238
	v_fma_f32 v230, v230, v238, v238
	v_fma_f32 v231, v231, v238, v238
	v_fma_f32 v232, v232, v238, v238
	v_fma_f32 v233, v233, v238, v238
	v_fma_f32 v234, v234, v238, v238
	v_fma_f32 v235, v235, v238, v238
	v_rcp_f32_e32 v228, v228
	v_rcp_f32_e32 v229, v229
	v_rcp_f32_e32 v230, v230
	v_rcp_f32_e32 v231, v231
	v_rcp_f32_e32 v232, v232
	v_rcp_f32_e32 v233, v233
	v_rcp_f32_e32 v234, v234
	v_rcp_f32_e32 v235, v235
	v_mul_f32_e32 v56, v64, v56
	v_mul_f32_e32 v57, v65, v57
	v_mul_f32_e32 v58, v66, v58
	v_mul_f32_e32 v59, v67, v59
	v_mul_f32_e32 v52, v60, v52
	v_mul_f32_e32 v53, v61, v53
	v_mul_f32_e32 v54, v62, v54
	v_mul_f32_e32 v55, v63, v55
	s_mov_b64 s[0:1], 0xb0000
	v_lshl_add_u64 v[242:243], v[240:241], 0, s[0:1]
	v_mul_f32_e32 v64, v56, v228
	v_mul_f32_e32 v65, v57, v229
	v_mul_f32_e32 v66, v58, v230
	v_mul_f32_e32 v67, v59, v231
	v_mul_f32_e32 v60, v52, v232
	v_mul_f32_e32 v61, v53, v233
	v_mul_f32_e32 v62, v54, v234
	v_mul_f32_e32 v63, v55, v235
	v_cvt_pk_bf16_f32 v64, v64, v65
	v_cvt_pk_bf16_f32 v65, v66, v67
	v_cvt_pk_bf16_f32 v66, v60, v61
	v_cvt_pk_bf16_f32 v67, v62, v63
	global_store_dwordx4 v[242:243], v[64:67], off
	s_waitcnt lgkmcnt(0)
	v_mov_b32_e32 v236, v239
	ds_read_b32 v239, v148 offset:640
	v_mul_f32_e32 v237, 0xbfb8aa3b, v236
	v_mul_f32_e32 v238, v236, v236
	v_rcp_f32_e32 v238, v238
	v_mul_f32_e32 v228, v237, v48
	v_mul_f32_e32 v229, v237, v49
	v_mul_f32_e32 v230, v237, v50
	v_mul_f32_e32 v231, v237, v51
	v_mul_f32_e32 v232, v237, v44
	v_mul_f32_e32 v233, v237, v45
	v_mul_f32_e32 v234, v237, v46
	v_mul_f32_e32 v235, v237, v47
	v_exp_f32_e32 v228, v228
	v_exp_f32_e32 v229, v229
	v_exp_f32_e32 v230, v230
	v_exp_f32_e32 v231, v231
	v_exp_f32_e32 v232, v232
	v_exp_f32_e32 v233, v233
	v_exp_f32_e32 v234, v234
	v_exp_f32_e32 v235, v235
	v_fma_f32 v228, v228, v238, v238
	v_fma_f32 v229, v229, v238, v238
	v_fma_f32 v230, v230, v238, v238
	v_fma_f32 v231, v231, v238, v238
	v_fma_f32 v232, v232, v238, v238
	v_fma_f32 v233, v233, v238, v238
	v_fma_f32 v234, v234, v238, v238
	v_fma_f32 v235, v235, v238, v238
	v_rcp_f32_e32 v228, v228
	v_rcp_f32_e32 v229, v229
	v_rcp_f32_e32 v230, v230
	v_rcp_f32_e32 v231, v231
	v_rcp_f32_e32 v232, v232
	v_rcp_f32_e32 v233, v233
	v_rcp_f32_e32 v234, v234
	v_rcp_f32_e32 v235, v235
	v_mul_f32_e32 v40, v48, v40
	v_mul_f32_e32 v41, v49, v41
	v_mul_f32_e32 v42, v50, v42
	v_mul_f32_e32 v43, v51, v43
	v_mul_f32_e32 v36, v44, v36
	v_mul_f32_e32 v37, v45, v37
	v_mul_f32_e32 v38, v46, v38
	v_mul_f32_e32 v39, v47, v39
	s_mov_b64 s[0:1], 0xc6000
	v_lshl_add_u64 v[242:243], v[240:241], 0, s[0:1]
	v_mul_f32_e32 v48, v40, v228
	v_mul_f32_e32 v49, v41, v229
	v_mul_f32_e32 v50, v42, v230
	v_mul_f32_e32 v51, v43, v231
	v_mul_f32_e32 v44, v36, v232
	v_mul_f32_e32 v45, v37, v233
	v_mul_f32_e32 v46, v38, v234
	v_mul_f32_e32 v47, v39, v235
	v_cvt_pk_bf16_f32 v48, v48, v49
	v_cvt_pk_bf16_f32 v49, v50, v51
	v_cvt_pk_bf16_f32 v50, v44, v45
	v_cvt_pk_bf16_f32 v51, v46, v47
	global_store_dwordx4 v[242:243], v[48:51], off
	s_waitcnt lgkmcnt(0)
; #define PG8_LAS __attribute__((address_space(3)))
; __device__ __forceinline__ float sigm(float x) { return __builtin_amdgcn_rcpf(1.0f + __builtin_amdgcn_exp2f(-1.4426950408889634f * x)); }
; __device__ __forceinline__ u32x4 pack8(const f32x4 a, const f32x4 b) { u32x4 w; w.x = cvt_pk_bf16(a[0], a[1]); w.y = cvt_pk_bf16(a[2], a[3]); w.z = cvt_pk_bf16(b[0], b[1]); w.w = cvt_pk_bf16(b[2], b[3]); return w; }
; #define PG8_WAIT_V(n) asm volatile("s_waitcnt vmcnt(" #n ")" ::: "memory")
; #define PG8_BAR __builtin_amdgcn_s_barrier()
;     __device__ __forceinline__ void operator()(const f32x4 (&acc)[2][2][4][2], const Unit& u, int wr, int wc, int fr, int fq) const {
;         const int rl0 = wr * 64 + fr + (u.half == 2 ? HALF : 0), row0 = u.pm * BM + rl0, col0 = u.pn * HALF + wc * 32 + 8 * fq; const PG8_LAS float* rsr = rsl + rl0;
; #pragma unroll
;         for (int ai = 0; ai < 2; ++ai) { if (ai == 1 && u.half != 0) break;
; #pragma unroll
;             for (int m = 0; m < 4; ++m) { const float rf = rsr[ai * HALF + m * 16]; f32x4 v0 = acc[ai][0][m][0] * rf, v1 = acc[ai][0][m][1] * rf; const f32x4 u0 = acc[ai][1][m][0] * rf, u1 = acc[ai][1][m][1] * rf;
; #pragma unroll
;                 for (int e = 0; e < 4; ++e) { v0[e] = v0[e] * sigm(v0[e]) * u0[e]; v1[e] = v1[e] * sigm(v1[e]) * u1[e]; }
;                 *(u32x4*)(H + (size_t)(row0 + ai * HALF + m * 16) * DFF + col0) = pack8(v0, v1); } }
;     }
; template <class Epi, class Sched, bool ALIGN_EPI = false, bool SP2 = false>
; __device__ __forceinline__ void gemm_phase(PG8_LAS unsigned char* lds, const Gemm g, const Sched& S, const Epi& E) {
;     ...
;     PG8_WAIT_V(0);
;     if constexpr (!ALIGN_EPI) { if (wr == 0) PG8_BAR; }
;     PG8_BAR;
	v_mov_b32_e32 v236, v239
	ds_read_b32 v239, v148 offset:704
	v_mul_f32_e32 v237, 0xbfb8aa3b, v236
	v_mul_f32_e32 v238, v236, v236
	v_rcp_f32_e32 v238, v238
	v_mul_f32_e32 v228, v237, v32
	v_mul_f32_e32 v229, v237, v33
	v_mul_f32_e32 v230, v237, v34
	v_mul_f32_e32 v231, v237, v35
	v_mul_f32_e32 v232, v237, v28
	v_mul_f32_e32 v233, v237, v29
	v_mul_f32_e32 v234, v237, v30
	v_mul_f32_e32 v235, v237, v31
	v_exp_f32_e32 v228, v228
	v_exp_f32_e32 v229, v229
	v_exp_f32_e32 v230, v230
	v_exp_f32_e32 v231, v231
	v_exp_f32_e32 v232, v232
	v_exp_f32_e32 v233, v233
	v_exp_f32_e32 v234, v234
	v_exp_f32_e32 v235, v235
	v_fma_f32 v228, v228, v238, v238
	v_fma_f32 v229, v229, v238, v238
	v_fma_f32 v230, v230, v238, v238
	v_fma_f32 v231, v231, v238, v238
	v_fma_f32 v232, v232, v238, v238
	v_fma_f32 v233, v233, v238, v238
	v_fma_f32 v234, v234, v238, v238
	v_fma_f32 v235, v235, v238, v238
	v_rcp_f32_e32 v228, v228
	v_rcp_f32_e32 v229, v229
	v_rcp_f32_e32 v230, v230
	v_rcp_f32_e32 v231, v231
	v_rcp_f32_e32 v232, v232
	v_rcp_f32_e32 v233, v233
	v_rcp_f32_e32 v234, v234
	v_rcp_f32_e32 v235, v235
	v_mul_f32_e32 v24, v32, v24
	v_mul_f32_e32 v25, v33, v25
	v_mul_f32_e32 v26, v34, v26
	v_mul_f32_e32 v27, v35, v27
	v_mul_f32_e32 v20, v28, v20
	v_mul_f32_e32 v21, v29, v21
	v_mul_f32_e32 v22, v30, v22
	v_mul_f32_e32 v23, v31, v23
	s_mov_b64 s[0:1], 0xdc000
	v_lshl_add_u64 v[242:243], v[240:241], 0, s[0:1]
	v_mul_f32_e32 v32, v24, v228
	v_mul_f32_e32 v33, v25, v229
	v_mul_f32_e32 v34, v26, v230
	v_mul_f32_e32 v35, v27, v231
	v_mul_f32_e32 v28, v20, v232
	v_mul_f32_e32 v29, v21, v233
	v_mul_f32_e32 v30, v22, v234
	v_mul_f32_e32 v31, v23, v235
	v_cvt_pk_bf16_f32 v32, v32, v33
	v_cvt_pk_bf16_f32 v33, v34, v35
	v_cvt_pk_bf16_f32 v34, v28, v29
	v_cvt_pk_bf16_f32 v35, v30, v31
	global_store_dwordx4 v[242:243], v[32:35], off
	s_waitcnt lgkmcnt(0)
	v_mov_b32_e32 v236, v239
	v_mul_f32_e32 v237, 0xbfb8aa3b, v236
	v_mul_f32_e32 v238, v236, v236
	v_rcp_f32_e32 v238, v238
	v_mul_f32_e32 v228, v237, v16
	v_mul_f32_e32 v229, v237, v17
	v_mul_f32_e32 v230, v237, v18
	v_mul_f32_e32 v231, v237, v19
	v_mul_f32_e32 v232, v237, v12
	v_mul_f32_e32 v233, v237, v13
	v_mul_f32_e32 v234, v237, v14
	v_mul_f32_e32 v235, v237, v15
	v_exp_f32_e32 v228, v228
	v_exp_f32_e32 v229, v229
	v_exp_f32_e32 v230, v230
	v_exp_f32_e32 v231, v231
	v_exp_f32_e32 v232, v232
	v_exp_f32_e32 v233, v233
	v_exp_f32_e32 v234, v234
	v_exp_f32_e32 v235, v235
	v_fma_f32 v228, v228, v238, v238
	v_fma_f32 v229, v229, v238, v238
	v_fma_f32 v230, v230, v238, v238
	v_fma_f32 v231, v231, v238, v238
	v_fma_f32 v232, v232, v238, v238
	v_fma_f32 v233, v233, v238, v238
	v_fma_f32 v234, v234, v238, v238
	v_fma_f32 v235, v235, v238, v238
	v_rcp_f32_e32 v228, v228
	v_rcp_f32_e32 v229, v229
	v_rcp_f32_e32 v230, v230
	v_rcp_f32_e32 v231, v231
	v_rcp_f32_e32 v232, v232
	v_rcp_f32_e32 v233, v233
	v_rcp_f32_e32 v234, v234
	v_rcp_f32_e32 v235, v235
	v_mul_f32_e32 v8, v16, v8
	v_mul_f32_e32 v9, v17, v9
	v_mul_f32_e32 v10, v18, v10
	v_mul_f32_e32 v11, v19, v11
	v_mul_f32_e32 v4, v12, v4
	v_mul_f32_e32 v5, v13, v5
	v_mul_f32_e32 v6, v14, v6
	v_mul_f32_e32 v7, v15, v7
	s_mov_b64 s[0:1], 0xf2000
	v_lshl_add_u64 v[242:243], v[240:241], 0, s[0:1]
	v_mul_f32_e32 v16, v8, v228
	v_mul_f32_e32 v17, v9, v229
	v_mul_f32_e32 v18, v10, v230
	v_mul_f32_e32 v19, v11, v231
	v_mul_f32_e32 v12, v4, v232
	v_mul_f32_e32 v13, v5, v233
	v_mul_f32_e32 v14, v6, v234
	v_mul_f32_e32 v15, v7, v235
	v_cvt_pk_bf16_f32 v16, v16, v17
	v_cvt_pk_bf16_f32 v17, v18, v19
	v_cvt_pk_bf16_f32 v18, v12, v13
	v_cvt_pk_bf16_f32 v19, v14, v15
	global_store_dwordx4 v[242:243], v[16:19], off
	s_andn2_b64 vcc, exec, s[38:39]
	s_mov_b64 s[0:1], -1
	s_cbranch_vccnz .LBB0_1473
	s_andn2_b64 vcc, exec, s[8:9]
	s_cbranch_vccnz .LBB0_1472
	s_branch .LBB0_1472
.LBB0_1483:
	s_waitcnt vmcnt(0)
	s_and_b64 vcc, exec, s[12:13]
	s_cbranch_vccz .Lgu_drain
	s_barrier
.Lgu_drain:
	s_barrier
